# baseline (speedup 1.0000x reference)
.LBB2_12:
	s_or_b32 s36, s1, s48
	v_or_b32_e32 v4, s36, v158
	v_mov_b32_e32 v5, v1
	v_lshlrev_b64 v[4:5], 7, v[4:5]
	v_lshl_add_u64 v[4:5], v[160:161], 0, v[4:5]
	global_load_dwordx4 v[122:125], v[4:5], off
	global_load_dwordx4 v[126:129], v[4:5], off offset:32
	global_load_dwordx4 v[130:133], v[4:5], off offset:64
	global_load_dwordx4 v[134:137], v[4:5], off offset:96
	s_waitcnt vmcnt(0)
	v_writelane_b32 v252, s36, 37
	s_sub_i32 s36, s36, s33
	s_waitcnt vmcnt(0) lgkmcnt(0)
	s_barrier
	s_and_b64 vcc, exec, s[38:39]
	s_cbranch_vccnz .Lmy_nodefer
	v_readlane_b32 s37, v252, 15
	s_cmp_lg_u32 s37, 0
	s_cbranch_scc1 .Lmy_nodefer
	global_store_dwordx4 v[102:103], v[86:89], off
	global_store_dwordx4 v[102:103], v[90:93], off offset:32
	global_store_dwordx4 v[102:103], v[94:97], off offset:64
	global_store_dwordx4 v[102:103], v[98:101], off offset:96
.Lmy_nodefer:
	s_cmp_lt_i32 s36, 0
	s_cbranch_scc1 .LBB2_20
	s_lshl_b32 s36, s36, 7
	s_and_b32 s37, s36, 0x7000
	v_add_u32_e32 v2, s37, v176
	v_add_u32_e32 v4, v2, v177
	ds_read_b128 v[4:7], v4 offset:32768
	v_add_u32_e32 v8, v2, v178
	ds_read_b128 v[8:11], v8 offset:32768
	s_add_i32 s37, s36, 0x7000
	s_and_b32 s37, s37, 0x7000
	s_waitcnt lgkmcnt(1)
	v_mfma_f32_32x32x16_f16 v[20:35], v[122:125], v[4:7], 0
	v_add_u32_e32 v4, v2, v179
	ds_read_b128 v[4:7], v4 offset:32768
	v_add_u32_e32 v2, v2, v180
	s_addk_i32 s36, 0x6000
	s_and_b32 s36, s36, 0x7000
	v_add_u32_e32 v52, s36, v176
	v_add_u32_e32 v44, v52, v178
	s_waitcnt lgkmcnt(1)
	v_mfma_f32_32x32x16_f16 v[20:35], v[126:129], v[8:11], v[20:35]
	ds_read_b128 v[8:11], v2 offset:32768
	v_add_u32_e32 v2, s37, v176
	v_add_u32_e32 v40, v2, v178
	ds_read_b128 v[40:43], v40 offset:32768
	ds_read_b128 v[44:47], v44 offset:32768
	v_add_u32_e32 v48, v52, v179
	ds_read_b128 v[48:51], v48 offset:32768
	s_waitcnt lgkmcnt(4)
	v_mfma_f32_32x32x16_f16 v[20:35], v[130:133], v[4:7], v[20:35]
	v_add_u32_e32 v4, v2, v177
	ds_read_b128 v[4:7], v4 offset:32768
	s_waitcnt lgkmcnt(4)
	v_mfma_f32_32x32x16_f16 v[20:35], v[134:137], v[8:11], v[20:35]
	v_add_u32_e32 v8, v52, v177
	ds_read_b128 v[36:39], v8 offset:32768
	s_waitcnt lgkmcnt(1)
	v_mfma_f32_32x32x16_f16 v[4:19], v[122:125], v[4:7], 0
	v_mfma_f32_32x32x16_f16 v[4:19], v[126:129], v[40:43], v[4:19]
	v_add_u32_e32 v40, v2, v179
	ds_read_b128 v[40:43], v40 offset:32768
	v_add_u32_e32 v2, v2, v180
	s_waitcnt lgkmcnt(0)
	v_mfma_f32_32x32x16_f16 v[4:19], v[130:133], v[40:43], v[4:19]
	ds_read_b128 v[40:43], v2 offset:32768
	v_add_u32_e32 v2, v52, v180
	ds_read_b128 v[54:57], v2 offset:32768
	v_mfma_f32_32x32x16_f16 v[70:85], v[122:125], v[36:39], 0
	s_waitcnt lgkmcnt(1)
	v_mfma_f32_32x32x16_f16 v[4:19], v[134:137], v[40:43], v[4:19]
	v_mfma_f32_32x32x16_f16 v[70:85], v[126:129], v[44:47], v[70:85]
	s_nop 10
	v_cndmask_b32_e64 v2, v20, v4, s[52:53]
	ds_write_b32 v181, v2
	v_cndmask_b32_e64 v2, v21, v5, s[4:5]
	ds_write_b32 v181, v2 offset:128
	v_cndmask_b32_e64 v2, v22, v6, s[6:7]
	ds_write_b32 v181, v2 offset:256
	v_cndmask_b32_e64 v2, v23, v7, s[8:9]
	v_mfma_f32_32x32x16_f16 v[70:85], v[130:133], v[48:51], v[70:85]
	ds_write_b32 v181, v2 offset:384
	v_cndmask_b32_e64 v2, v24, v8, s[10:11]
	ds_write_b32 v181, v2 offset:1024
	v_cndmask_b32_e64 v2, v25, v9, s[12:13]
	ds_write_b32 v181, v2 offset:1152
	v_cndmask_b32_e64 v2, v26, v10, s[14:15]
	ds_write_b32 v181, v2 offset:1280
	v_cndmask_b32_e64 v2, v27, v11, s[16:17]
	ds_write_b32 v181, v2 offset:1408
	v_cndmask_b32_e64 v2, v28, v12, s[18:19]
	s_waitcnt lgkmcnt(8)
	v_mfma_f32_32x32x16_f16 v[70:85], v[134:137], v[54:57], v[70:85]
	ds_write_b32 v181, v2 offset:2048
	v_cndmask_b32_e64 v2, v29, v13, s[20:21]
	ds_write_b32 v181, v2 offset:2176
	v_cndmask_b32_e64 v2, v30, v14, s[22:23]
	ds_write_b32 v181, v2 offset:2304
	v_cndmask_b32_e64 v2, v31, v15, s[24:25]
	ds_write_b32 v181, v2 offset:2432
	v_cndmask_b32_e64 v2, v32, v16, s[26:27]
	ds_write_b32 v181, v2 offset:3072
	v_cndmask_b32_e64 v2, v33, v17, s[28:29]
	ds_write_b32 v181, v2 offset:3200
	v_cndmask_b32_e64 v2, v34, v18, s[30:31]
	ds_write_b32 v181, v2 offset:3328
	v_cndmask_b32_e64 v2, v35, v19, s[34:35]
	ds_write_b32 v181, v2 offset:3456
	v_cndmask_b32_e64 v2, v4, v70, s[52:53]
	ds_read_b32 v38, v214
	ds_read_b32 v39, v215
	ds_read_b32 v40, v216
	ds_read_b32 v41, v217
	ds_read_b32 v42, v218
	ds_read_b32 v43, v219
	ds_read_b32 v44, v220
	ds_read_b32 v45, v221
	ds_read_b32 v46, v222
	ds_read_b32 v47, v223
	ds_read_b32 v48, v224
	ds_read_b32 v49, v225
	ds_read_b32 v50, v226
	ds_read_b32 v51, v227
	ds_read_b32 v52, v228
	ds_read_b32 v53, v229
	ds_write_b32 v181, v2
	v_cndmask_b32_e64 v2, v5, v71, s[4:5]
	ds_write_b32 v181, v2 offset:128
	v_cndmask_b32_e64 v2, v6, v72, s[6:7]
	ds_write_b32 v181, v2 offset:256
	v_cndmask_b32_e64 v2, v7, v73, s[8:9]
	ds_write_b32 v181, v2 offset:384
	v_cndmask_b32_e64 v2, v8, v74, s[10:11]
	ds_write_b32 v181, v2 offset:1024
	v_cndmask_b32_e64 v2, v9, v75, s[12:13]
	ds_write_b32 v181, v2 offset:1152
	v_cndmask_b32_e64 v2, v10, v76, s[14:15]
	ds_write_b32 v181, v2 offset:1280
	v_cndmask_b32_e64 v2, v11, v77, s[16:17]
	ds_write_b32 v181, v2 offset:1408
	v_cndmask_b32_e64 v2, v12, v78, s[18:19]
	ds_write_b32 v181, v2 offset:2048
	v_cndmask_b32_e64 v2, v13, v79, s[20:21]
	ds_write_b32 v181, v2 offset:2176
	v_cndmask_b32_e64 v2, v14, v80, s[22:23]
	ds_write_b32 v181, v2 offset:2304
	v_cndmask_b32_e64 v2, v15, v81, s[24:25]
	ds_write_b32 v181, v2 offset:2432
	v_cndmask_b32_e64 v2, v16, v82, s[26:27]
	ds_write_b32 v181, v2 offset:3072
	v_cndmask_b32_e64 v2, v17, v83, s[28:29]
	ds_write_b32 v181, v2 offset:3200
	v_cndmask_b32_e64 v2, v18, v84, s[30:31]
	ds_write_b32 v181, v2 offset:3328
	v_cndmask_b32_e64 v2, v19, v85, s[34:35]
	ds_write_b32 v181, v2 offset:3456
	ds_read_b32 v54, v214
	ds_read_b32 v55, v215
	ds_read_b32 v56, v216
	ds_read_b32 v57, v217
	ds_read_b32 v58, v218
	ds_read_b32 v59, v219
	ds_read_b32 v60, v220
	ds_read_b32 v61, v221
	ds_read_b32 v62, v222
	ds_read_b32 v63, v223
	ds_read_b32 v64, v224
	ds_read_b32 v65, v225
	ds_read_b32 v66, v226
	ds_read_b32 v67, v227
	ds_read_b32 v68, v228
	ds_read_b32 v69, v229
	s_branch .LBB2_21

.LBB2_57:
	v_readlane_b32 s44, v252, 28
	v_readlane_b32 s45, v252, 29
	s_andn2_b64 vcc, exec, s[44:45]
	v_readlane_b32 s48, v252, 33
	v_readlane_b32 s49, v252, 34
	v_readlane_b32 s50, v252, 35
	s_waitcnt lgkmcnt(0)
	s_barrier
	s_cbranch_vccnz .LBB2_1
	ds_read2st64_b32 v[4:5], v207 offset0:128 offset1:132
	v_max_f32_e32 v2, v232, v232
	ds_read2st64_b32 v[44:45], v207 offset0:64 offset1:68
	s_waitcnt lgkmcnt(1)
	v_max_f32_e32 v38, v4, v4
	v_max_f32_e32 v2, v2, v38
	v_sub_f32_e32 v38, v232, v2
	v_sub_f32_e32 v2, v4, v2
	v_exp_f32_e32 v39, v2
	v_exp_f32_e32 v38, v38
	v_mov_b32_e32 v165, v5
	v_mul_f32_e32 v2, v5, v39
	v_pk_fma_f32 v[4:5], v[164:165], v[38:39], v[2:3] op_sel_hi:[1,1,0]
	s_nop 0
	v_mov_b32_e32 v2, v4
	s_nop 1
	v_permlane32_swap_b32_e32 v4, v2
	v_add_f32_e32 v2, v4, v2
	v_div_scale_f32 v4, s[0:1], v2, v2, 1.0
	v_rcp_f32_e32 v5, v4
	v_div_scale_f32 v40, vcc, 1.0, v2, 1.0
	v_readlane_b32 s0, v252, 37
	v_fma_f32 v41, -v4, v5, 1.0
	v_fmac_f32_e32 v5, v41, v5
	v_mul_f32_e32 v41, v40, v5
	v_fma_f32 v42, -v4, v41, v40
	v_fmac_f32_e32 v41, v42, v5
	v_fma_f32 v4, -v4, v41, v40
	v_div_fmas_f32 v4, v4, v5, v41
	v_div_fixup_f32 v2, v4, v2, 1.0
	v_mul_f32_e32 v4, v38, v2
	v_mul_f32_e32 v38, v39, v2
	v_or_b32_e32 v2, s0, v0
	v_lshlrev_b64 v[42:43], 11, v[2:3]
	v_lshl_add_u64 v[42:43], v[162:163], 0, v[42:43]
	v_lshlrev_b32_e32 v2, 1, v159
	v_lshl_add_u64 v[42:43], v[42:43], 0, v[2:3]
	ds_read2st64_b32 v[86:87], v207 offset1:4
	ds_read2st64_b32 v[88:89], v207 offset0:8 offset1:12
	ds_read2st64_b32 v[90:91], v207 offset0:16 offset1:20
	ds_read2st64_b32 v[92:93], v207 offset0:24 offset1:28
	ds_read2st64_b32 v[94:95], v207 offset0:32 offset1:36
	ds_read2st64_b32 v[96:97], v207 offset0:40 offset1:44
	ds_read2st64_b32 v[98:99], v207 offset0:48 offset1:52
	ds_read2st64_b32 v[100:101], v207 offset0:56 offset1:60
	s_waitcnt lgkmcnt(7)
	v_pk_mul_f32 v[86:87], v[38:39], v[86:87] op_sel_hi:[0,1]
	v_pk_fma_f32 v[22:23], v[4:5], v[22:23], v[86:87] op_sel_hi:[0,1,1]
	s_waitcnt lgkmcnt(6)
	v_pk_mul_f32 v[88:89], v[38:39], v[88:89] op_sel_hi:[0,1]
	v_pk_fma_f32 v[24:25], v[4:5], v[24:25], v[88:89] op_sel_hi:[0,1,1]
	s_waitcnt lgkmcnt(5)
	v_pk_mul_f32 v[90:91], v[38:39], v[90:91] op_sel_hi:[0,1]
	v_pk_fma_f32 v[26:27], v[4:5], v[26:27], v[90:91] op_sel_hi:[0,1,1]
	s_waitcnt lgkmcnt(4)
	v_pk_mul_f32 v[92:93], v[38:39], v[92:93] op_sel_hi:[0,1]
	v_pk_fma_f32 v[28:29], v[4:5], v[28:29], v[92:93] op_sel_hi:[0,1,1]
	s_waitcnt lgkmcnt(3)
	v_pk_mul_f32 v[94:95], v[38:39], v[94:95] op_sel_hi:[0,1]
	v_pk_fma_f32 v[30:31], v[4:5], v[30:31], v[94:95] op_sel_hi:[0,1,1]
	s_waitcnt lgkmcnt(2)
	v_pk_mul_f32 v[96:97], v[38:39], v[96:97] op_sel_hi:[0,1]
	v_pk_fma_f32 v[32:33], v[4:5], v[32:33], v[96:97] op_sel_hi:[0,1,1]
	s_waitcnt lgkmcnt(1)
	v_pk_mul_f32 v[98:99], v[38:39], v[98:99] op_sel_hi:[0,1]
	v_pk_fma_f32 v[34:35], v[4:5], v[34:35], v[98:99] op_sel_hi:[0,1,1]
	s_waitcnt lgkmcnt(0)
	v_pk_mul_f32 v[100:101], v[38:39], v[100:101] op_sel_hi:[0,1]
	v_pk_fma_f32 v[36:37], v[4:5], v[36:37], v[100:101] op_sel_hi:[0,1,1]
	ds_read2st64_b32 v[102:103], v207 offset0:64 offset1:68
	ds_read2st64_b32 v[104:105], v207 offset0:72 offset1:76
	ds_read2st64_b32 v[106:107], v207 offset0:80 offset1:84
	ds_read2st64_b32 v[108:109], v207 offset0:88 offset1:92
	ds_read2st64_b32 v[110:111], v207 offset0:96 offset1:100
	ds_read2st64_b32 v[112:113], v207 offset0:104 offset1:108
	ds_read2st64_b32 v[114:115], v207 offset0:112 offset1:116
	ds_read2st64_b32 v[116:117], v207 offset0:120 offset1:124
	s_waitcnt lgkmcnt(7)
	v_pk_mul_f32 v[102:103], v[38:39], v[102:103] op_sel_hi:[0,1]
	v_pk_fma_f32 v[6:7], v[4:5], v[6:7], v[102:103] op_sel_hi:[0,1,1]
	s_waitcnt lgkmcnt(6)
	v_pk_mul_f32 v[104:105], v[38:39], v[104:105] op_sel_hi:[0,1]
	v_pk_fma_f32 v[8:9], v[4:5], v[8:9], v[104:105] op_sel_hi:[0,1,1]
	s_waitcnt lgkmcnt(5)
	v_pk_mul_f32 v[106:107], v[38:39], v[106:107] op_sel_hi:[0,1]
	v_pk_fma_f32 v[10:11], v[4:5], v[10:11], v[106:107] op_sel_hi:[0,1,1]
	s_waitcnt lgkmcnt(4)
	v_pk_mul_f32 v[108:109], v[38:39], v[108:109] op_sel_hi:[0,1]
	v_pk_fma_f32 v[12:13], v[4:5], v[12:13], v[108:109] op_sel_hi:[0,1,1]
	s_waitcnt lgkmcnt(3)
	v_pk_mul_f32 v[110:111], v[38:39], v[110:111] op_sel_hi:[0,1]
	v_pk_fma_f32 v[14:15], v[4:5], v[14:15], v[110:111] op_sel_hi:[0,1,1]
	s_waitcnt lgkmcnt(2)
	v_pk_mul_f32 v[112:113], v[38:39], v[112:113] op_sel_hi:[0,1]
	v_pk_fma_f32 v[16:17], v[4:5], v[16:17], v[112:113] op_sel_hi:[0,1,1]
	s_waitcnt lgkmcnt(1)
	v_pk_mul_f32 v[114:115], v[38:39], v[114:115] op_sel_hi:[0,1]
	v_pk_fma_f32 v[18:19], v[4:5], v[18:19], v[114:115] op_sel_hi:[0,1,1]
	s_waitcnt lgkmcnt(0)
	v_pk_mul_f32 v[116:117], v[38:39], v[116:117] op_sel_hi:[0,1]
	v_pk_fma_f32 v[20:21], v[4:5], v[20:21], v[116:117] op_sel_hi:[0,1,1]
	v_cvt_pk_f16_f32 v22, v22, v23
	v_cvt_pk_f16_f32 v23, v24, v25
	v_cvt_pk_f16_f32 v24, v26, v27
	v_cvt_pk_f16_f32 v25, v28, v29
	v_cvt_pk_f16_f32 v30, v30, v31
	v_cvt_pk_f16_f32 v31, v32, v33
	v_cvt_pk_f16_f32 v32, v34, v35
	v_cvt_pk_f16_f32 v33, v36, v37
	v_cvt_pk_f16_f32 v6, v6, v7
	v_cvt_pk_f16_f32 v7, v8, v9
	v_cvt_pk_f16_f32 v8, v10, v11
	v_cvt_pk_f16_f32 v9, v12, v13
	v_cvt_pk_f16_f32 v14, v14, v15
	v_cvt_pk_f16_f32 v15, v16, v17
	v_cvt_pk_f16_f32 v16, v18, v19
	v_cvt_pk_f16_f32 v17, v20, v21
	s_nop 1
	v_permlane32_swap_b32_e32 v22, v24
	v_permlane32_swap_b32_e32 v23, v25
	v_permlane32_swap_b32_e32 v30, v32
	v_permlane32_swap_b32_e32 v31, v33
	v_permlane32_swap_b32_e32 v6, v8
	v_permlane32_swap_b32_e32 v7, v9
	v_permlane32_swap_b32_e32 v14, v16
	v_permlane32_swap_b32_e32 v15, v17
	v_readlane_b32 s36, v252, 38
	s_cmp_lg_u32 s36, 0
	s_cbranch_scc1 .Lmy_store_now
	v_mov_b32_e32 v86, v22
	v_mov_b32_e32 v87, v23
	v_mov_b32_e32 v88, v24
	v_mov_b32_e32 v89, v25
	v_mov_b32_e32 v90, v30
	v_mov_b32_e32 v91, v31
	v_mov_b32_e32 v92, v32
	v_mov_b32_e32 v93, v33
	v_mov_b32_e32 v94, v6
	v_mov_b32_e32 v95, v7
	v_mov_b32_e32 v96, v8
	v_mov_b32_e32 v97, v9
	v_mov_b32_e32 v98, v14
	v_mov_b32_e32 v99, v15
	v_mov_b32_e32 v100, v16
	v_mov_b32_e32 v101, v17
	v_mov_b32_e32 v102, v42
	v_mov_b32_e32 v103, v43
	s_branch .LBB2_1
.Lmy_store_now:
	global_store_dwordx4 v[42:43], v[22:25], off
	global_store_dwordx4 v[42:43], v[30:33], off offset:32
	global_store_dwordx4 v[42:43], v[6:9], off offset:64
	global_store_dwordx4 v[42:43], v[14:17], off offset:96
	s_branch .LBB2_1
